# v91 + init phase: the 16-iteration router-table dot-product loop (3 loads + vmcnt(0) per iteration on 16 workgroups) unrolled: all 48 loads issued first, counted waits
# speedup vs baseline: 1.0052x; 1.0052x over previous
.LBB0_24:
	global_load_dword v100, v[6:7], off
	global_load_dword v102, v[12:13], off
	global_load_dword v103, v[10:11], off
	v_lshl_add_u64 v[6:7], v[6:7], 0, s[30:31]
	global_load_dword v104, v[6:7], off
	global_load_dword v106, v[12:13], off offset:256
	global_load_dword v107, v[10:11], off offset:256
	v_lshl_add_u64 v[6:7], v[6:7], 0, s[30:31]
	global_load_dword v108, v[6:7], off
	global_load_dword v110, v[12:13], off offset:512
	global_load_dword v111, v[10:11], off offset:512
	v_lshl_add_u64 v[6:7], v[6:7], 0, s[30:31]
	global_load_dword v112, v[6:7], off
	global_load_dword v114, v[12:13], off offset:768
	global_load_dword v115, v[10:11], off offset:768
	v_lshl_add_u64 v[6:7], v[6:7], 0, s[30:31]
	global_load_dword v116, v[6:7], off
	global_load_dword v118, v[12:13], off offset:1024
	global_load_dword v119, v[10:11], off offset:1024
	v_lshl_add_u64 v[6:7], v[6:7], 0, s[30:31]
	global_load_dword v120, v[6:7], off
	global_load_dword v122, v[12:13], off offset:1280
	global_load_dword v123, v[10:11], off offset:1280
	v_lshl_add_u64 v[6:7], v[6:7], 0, s[30:31]
	global_load_dword v124, v[6:7], off
	global_load_dword v126, v[12:13], off offset:1536
	global_load_dword v127, v[10:11], off offset:1536
	v_lshl_add_u64 v[6:7], v[6:7], 0, s[30:31]
	global_load_dword v128, v[6:7], off
	global_load_dword v130, v[12:13], off offset:1792
	global_load_dword v131, v[10:11], off offset:1792
	v_lshl_add_u64 v[6:7], v[6:7], 0, s[30:31]
	global_load_dword v132, v[6:7], off
	global_load_dword v134, v[12:13], off offset:2048
	global_load_dword v135, v[10:11], off offset:2048
	v_lshl_add_u64 v[6:7], v[6:7], 0, s[30:31]
	global_load_dword v136, v[6:7], off
	global_load_dword v138, v[12:13], off offset:2304
	global_load_dword v139, v[10:11], off offset:2304
	v_lshl_add_u64 v[6:7], v[6:7], 0, s[30:31]
	global_load_dword v140, v[6:7], off
	global_load_dword v142, v[12:13], off offset:2560
	global_load_dword v143, v[10:11], off offset:2560
	v_lshl_add_u64 v[6:7], v[6:7], 0, s[30:31]
	global_load_dword v144, v[6:7], off
	global_load_dword v146, v[12:13], off offset:2816
	global_load_dword v147, v[10:11], off offset:2816
	v_lshl_add_u64 v[6:7], v[6:7], 0, s[30:31]
	global_load_dword v148, v[6:7], off
	global_load_dword v150, v[12:13], off offset:3072
	global_load_dword v151, v[10:11], off offset:3072
	v_lshl_add_u64 v[6:7], v[6:7], 0, s[30:31]
	global_load_dword v152, v[6:7], off
	global_load_dword v154, v[12:13], off offset:3328
	global_load_dword v155, v[10:11], off offset:3328
	v_lshl_add_u64 v[6:7], v[6:7], 0, s[30:31]
	global_load_dword v156, v[6:7], off
	global_load_dword v158, v[12:13], off offset:3584
	global_load_dword v159, v[10:11], off offset:3584
	v_lshl_add_u64 v[6:7], v[6:7], 0, s[30:31]
	global_load_dword v160, v[6:7], off
	global_load_dword v162, v[12:13], off offset:3840
	global_load_dword v163, v[10:11], off offset:3840
	s_waitcnt vmcnt(45)
	v_pk_fma_f32 v[8:9], v[100:101], v[102:103], v[8:9] op_sel_hi:[0,1,1]
	s_waitcnt vmcnt(42)
	v_pk_fma_f32 v[8:9], v[104:105], v[106:107], v[8:9] op_sel_hi:[0,1,1]
	s_waitcnt vmcnt(39)
	v_pk_fma_f32 v[8:9], v[108:109], v[110:111], v[8:9] op_sel_hi:[0,1,1]
	s_waitcnt vmcnt(36)
	v_pk_fma_f32 v[8:9], v[112:113], v[114:115], v[8:9] op_sel_hi:[0,1,1]
	s_waitcnt vmcnt(33)
	v_pk_fma_f32 v[8:9], v[116:117], v[118:119], v[8:9] op_sel_hi:[0,1,1]
	s_waitcnt vmcnt(30)
	v_pk_fma_f32 v[8:9], v[120:121], v[122:123], v[8:9] op_sel_hi:[0,1,1]
	s_waitcnt vmcnt(27)
	v_pk_fma_f32 v[8:9], v[124:125], v[126:127], v[8:9] op_sel_hi:[0,1,1]
	s_waitcnt vmcnt(24)
	v_pk_fma_f32 v[8:9], v[128:129], v[130:131], v[8:9] op_sel_hi:[0,1,1]
	s_waitcnt vmcnt(21)
	v_pk_fma_f32 v[8:9], v[132:133], v[134:135], v[8:9] op_sel_hi:[0,1,1]
	s_waitcnt vmcnt(18)
	v_pk_fma_f32 v[8:9], v[136:137], v[138:139], v[8:9] op_sel_hi:[0,1,1]
	s_waitcnt vmcnt(15)
	v_pk_fma_f32 v[8:9], v[140:141], v[142:143], v[8:9] op_sel_hi:[0,1,1]
	s_waitcnt vmcnt(12)
	v_pk_fma_f32 v[8:9], v[144:145], v[146:147], v[8:9] op_sel_hi:[0,1,1]
	s_waitcnt vmcnt(9)
	v_pk_fma_f32 v[8:9], v[148:149], v[150:151], v[8:9] op_sel_hi:[0,1,1]
	s_waitcnt vmcnt(6)
	v_pk_fma_f32 v[8:9], v[152:153], v[154:155], v[8:9] op_sel_hi:[0,1,1]
	s_waitcnt vmcnt(3)
	v_pk_fma_f32 v[8:9], v[156:157], v[158:159], v[8:9] op_sel_hi:[0,1,1]
	s_waitcnt vmcnt(0)
	v_pk_fma_f32 v[8:9], v[160:161], v[162:163], v[8:9] op_sel_hi:[0,1,1]
	s_or_b64 exec, exec, s[2:3]
	ds_bpermute_b32 v4, v1, v8
	ds_bpermute_b32 v6, v1, v9
	s_waitcnt lgkmcnt(1)
	v_add_f32_e32 v4, v8, v4
	s_waitcnt lgkmcnt(0)
	v_add_f32_e32 v6, v9, v6
	ds_bpermute_b32 v7, v15, v4
	ds_bpermute_b32 v8, v15, v6
	s_waitcnt lgkmcnt(1)
	v_add_f32_e32 v4, v4, v7
	s_waitcnt lgkmcnt(0)
	v_add_f32_e32 v6, v6, v8
	ds_bpermute_b32 v7, v16, v4
	ds_bpermute_b32 v8, v16, v6
	s_waitcnt lgkmcnt(1)
	v_add_f32_e32 v4, v4, v7
	s_waitcnt lgkmcnt(0)
	v_add_f32_e32 v6, v6, v8
	ds_bpermute_b32 v7, v17, v4
	ds_bpermute_b32 v8, v17, v6
	s_waitcnt lgkmcnt(1)
	v_add_f32_e32 v4, v4, v7
	s_waitcnt lgkmcnt(0)
	v_add_f32_e32 v6, v6, v8
	ds_bpermute_b32 v7, v18, v4
	ds_bpermute_b32 v8, v18, v6
	s_waitcnt lgkmcnt(1)
	v_add_f32_e32 v4, v4, v7
	s_waitcnt lgkmcnt(0)
	v_add_f32_e32 v7, v6, v8
	ds_bpermute_b32 v6, v19, v4
	ds_bpermute_b32 v8, v19, v7
	s_and_saveexec_b64 s[2:3], vcc
	s_cbranch_execz .LBB0_22
	s_and_b32 s4, s35, 31
	s_lshl_b32 s5, s39, 6
	s_or_b32 s4, s5, s4
	s_ashr_i32 s5, s4, 31
	s_lshl_b64 s[4:5], s[4:5], 2
	s_add_u32 s4, s25, s4
	s_addc_u32 s5, s36, s5
	s_waitcnt lgkmcnt(1)
	v_add_f32_e32 v4, v4, v6
	s_waitcnt lgkmcnt(0)
	v_add_f32_e32 v7, v7, v8
	global_store_dword v5, v4, s[4:5]
	global_store_dword v5, v7, s[4:5] offset:128
	s_branch .LBB0_22
